# v060 + the same gate-load hoist in the layer-0 down-projection's ctx (split-K) unit epilogue
# baseline (speedup 1.0000x reference)
; __device__ __forceinline__ u32x4 pack8(const f32x4 a, const f32x4 b) { u32x4 w; w.x = cvt_pk_bf16(a[0], a[1]); w.y = cvt_pk_bf16(a[2], a[3]); w.z = cvt_pk_bf16(b[0], b[1]); w.w = cvt_pk_bf16(b[2], b[3]); return w; }
;     __device__ __forceinline__ void operator()(const f32x4 (&acc)[2][2][4][2], const Unit& u, int wr, int wc, int fr, int fq) const {
;     ...
;         if (u.kq >= 0) {
;             if (wr == 0) {
; #pragma unroll
;                 for (int m = 0; m < 4; ++m) { const int row = row0 + m * 16; const float gsc = gvp[row];
; #pragma unroll
;                     for (int bj = 0; bj < 2; ++bj) *(u32x4*)(base + (size_t)(row + 64 * u.kq) * D + col0 + bj * HALF) = pack8(acc[0][bj][m][0] * gsc, acc[0][bj][m][1] * gsc); }
;             }
;             return;
.LBB0_1113:
	s_and_b64 vcc, exec, s[10:11]
	s_cbranch_vccz .LBB0_1115
	v_ashrrev_i32_e32 v5, 31, v4
	v_lshl_add_u64 v[70:71], v[4:5], 2, s[8:9]
	global_load_dword v162, v[70:71], off
	global_load_dword v164, v[70:71], off offset:64
	global_load_dword v174, v[70:71], off offset:128
	global_load_dword v176, v[70:71], off offset:192
	v_lshl_add_u32 v4, s45, 6, v4
	v_ashrrev_i32_e32 v135, 31, v134
	v_ashrrev_i32_e32 v5, 31, v4
	v_lshl_add_u64 v[74:75], v[134:135], 1, s[6:7]
	v_lshlrev_b64 v[76:77], 11, v[4:5]
	v_lshl_add_u64 v[76:77], v[74:75], 0, v[76:77]
	s_mov_b64 s[4:5], -1
	s_waitcnt vmcnt(3)
	v_pk_mul_f32 v[68:69], v[68:69], v[162:163] op_sel_hi:[1,0]
	v_pk_mul_f32 v[66:67], v[66:67], v[162:163] op_sel_hi:[1,0]
	v_pk_mul_f32 v[64:65], v[64:65], v[162:163] op_sel_hi:[1,0]
	v_pk_mul_f32 v[62:63], v[62:63], v[162:163] op_sel_hi:[1,0]
	v_pk_mul_f32 v[60:61], v[60:61], v[162:163] op_sel_hi:[1,0]
	v_pk_mul_f32 v[58:59], v[58:59], v[162:163] op_sel_hi:[1,0]
	v_pk_mul_f32 v[78:79], v[56:57], v[162:163] op_sel_hi:[1,0]
	v_pk_mul_f32 v[72:73], v[54:55], v[162:163] op_sel_hi:[1,0]
	v_cvt_pk_bf16_f32 v54, v66, v67
	v_cvt_pk_bf16_f32 v55, v68, v69
	v_cvt_pk_bf16_f32 v56, v62, v63
	v_cvt_pk_bf16_f32 v57, v64, v65
	v_cvt_pk_bf16_f32 v58, v58, v59
	v_cvt_pk_bf16_f32 v59, v60, v61
	v_cvt_pk_bf16_f32 v60, v72, v73
	v_cvt_pk_bf16_f32 v61, v78, v79
	global_store_dwordx4 v[76:77], v[54:57], off
	global_store_dwordx4 v[76:77], v[58:61], off offset:256
	v_add_u32_e32 v56, 16, v4
	v_ashrrev_i32_e32 v57, 31, v56
	v_lshlrev_b64 v[56:57], 11, v[56:57]
	v_lshl_add_u64 v[56:57], v[74:75], 0, v[56:57]
	s_waitcnt vmcnt(4)
	v_pk_mul_f32 v[52:53], v[52:53], v[164:165] op_sel_hi:[1,0]
	v_pk_mul_f32 v[50:51], v[50:51], v[164:165] op_sel_hi:[1,0]
	v_pk_mul_f32 v[48:49], v[48:49], v[164:165] op_sel_hi:[1,0]
	v_pk_mul_f32 v[46:47], v[46:47], v[164:165] op_sel_hi:[1,0]
	v_pk_mul_f32 v[44:45], v[44:45], v[164:165] op_sel_hi:[1,0]
	v_pk_mul_f32 v[42:43], v[42:43], v[164:165] op_sel_hi:[1,0]
	v_pk_mul_f32 v[58:59], v[40:41], v[164:165] op_sel_hi:[1,0]
	v_pk_mul_f32 v[54:55], v[38:39], v[164:165] op_sel_hi:[1,0]
	v_cvt_pk_bf16_f32 v38, v50, v51
	v_cvt_pk_bf16_f32 v39, v52, v53
	v_cvt_pk_bf16_f32 v40, v46, v47
	v_cvt_pk_bf16_f32 v41, v48, v49
	v_cvt_pk_bf16_f32 v42, v42, v43
	v_cvt_pk_bf16_f32 v43, v44, v45
	v_cvt_pk_bf16_f32 v44, v54, v55
	v_cvt_pk_bf16_f32 v45, v58, v59
	global_store_dwordx4 v[56:57], v[38:41], off
	global_store_dwordx4 v[56:57], v[42:45], off offset:256
	v_add_u32_e32 v40, 32, v4
	v_ashrrev_i32_e32 v41, 31, v40
	v_lshlrev_b64 v[40:41], 11, v[40:41]
	v_lshl_add_u64 v[40:41], v[74:75], 0, v[40:41]
	v_add_u32_e32 v4, 48, v4
	v_ashrrev_i32_e32 v5, 31, v4
	v_lshlrev_b64 v[4:5], 11, v[4:5]
	v_lshl_add_u64 v[86:87], v[74:75], 0, v[4:5]
	s_waitcnt vmcnt(5)
	v_pk_mul_f32 v[36:37], v[36:37], v[174:175] op_sel_hi:[1,0]
	v_pk_mul_f32 v[34:35], v[34:35], v[174:175] op_sel_hi:[1,0]
	v_pk_mul_f32 v[32:33], v[32:33], v[174:175] op_sel_hi:[1,0]
	v_pk_mul_f32 v[30:31], v[30:31], v[174:175] op_sel_hi:[1,0]
	v_pk_mul_f32 v[28:29], v[28:29], v[174:175] op_sel_hi:[1,0]
	v_pk_mul_f32 v[26:27], v[26:27], v[174:175] op_sel_hi:[1,0]
	v_pk_mul_f32 v[42:43], v[24:25], v[174:175] op_sel_hi:[1,0]
	v_pk_mul_f32 v[38:39], v[22:23], v[174:175] op_sel_hi:[1,0]
	v_cvt_pk_bf16_f32 v22, v34, v35
	v_cvt_pk_bf16_f32 v23, v36, v37
	v_cvt_pk_bf16_f32 v24, v30, v31
	v_cvt_pk_bf16_f32 v25, v32, v33
	v_cvt_pk_bf16_f32 v26, v26, v27
	v_cvt_pk_bf16_f32 v27, v28, v29
	v_cvt_pk_bf16_f32 v28, v38, v39
	v_cvt_pk_bf16_f32 v29, v42, v43
	global_store_dwordx4 v[40:41], v[22:25], off
	global_store_dwordx4 v[40:41], v[26:29], off offset:256
	s_waitcnt vmcnt(6)
	v_pk_mul_f32 v[20:21], v[20:21], v[176:177] op_sel_hi:[1,0]
	v_pk_mul_f32 v[4:5], v[18:19], v[176:177] op_sel_hi:[1,0]
	v_pk_mul_f32 v[16:17], v[16:17], v[176:177] op_sel_hi:[1,0]
	v_pk_mul_f32 v[14:15], v[14:15], v[176:177] op_sel_hi:[1,0]
	v_pk_mul_f32 v[76:77], v[12:13], v[176:177] op_sel_hi:[1,0]
	v_pk_mul_f32 v[74:75], v[10:11], v[176:177] op_sel_hi:[1,0]
	v_pk_mul_f32 v[72:73], v[8:9], v[176:177] op_sel_hi:[1,0]
	v_pk_mul_f32 v[70:71], v[6:7], v[176:177] op_sel_hi:[1,0]
	v_cvt_pk_bf16_f32 v4, v4, v5
	v_cvt_pk_bf16_f32 v5, v20, v21
	v_cvt_pk_bf16_f32 v6, v14, v15
	v_cvt_pk_bf16_f32 v7, v16, v17
	global_store_dwordx4 v[86:87], v[4:7], off
